# attention second half-step QK^T: K-fragment LDS reads triple-buffered (v250-253 as third buffer), the two LDS-resident Q fragments prefetched into v242-245 / v182-185 at the top
# speedup vs baseline: 1.0101x; 1.0013x over previous
; __device__ __forceinline__ unsigned sel_bit_mask(unsigned w, int b) { unsigned m; asm("v_bfe_i32 %0, %1, %2, 1" : "=v"(m) : "v"(w), "n"(b)); return m; }
; template <bool SEL>
; __device__ __forceinline__ void partialSM(f32x16& p0, f32x16& p1, float& m_reg, float& mn, float& alpha, unsigned selw) {
;     ...
;     constexpr float C2 = 1.4426950408889634f * SCALE;
;     if (__builtin_expect(__all((pmax - m_reg) * SCALE <= THR), 1)) { mn = m_reg; alpha = 1.f; }
;     else { mn = fmaxf(m_reg, pmax); alpha = __builtin_amdgcn_exp2f((m_reg - mn) * C2); m_reg = mn; }
;     const float mnL = -mn * C2;
; #pragma unroll
;     for (int r = 0; r < 16; ++r) p0[r] = fmaf(p0[r], C2, mnL);
; #pragma unroll
;     for (int r = 0; r < 16; ++r) p1[r] = fmaf(p1[r], C2, mnL);
; #pragma unroll
;     for (int r = 0; r < 16; ++r) p0[r] = __builtin_amdgcn_exp2f(p0[r]);
;     if (SEL) {
; #pragma unroll
;         for (int r = 0; r < 16; ++r) p0[r] = __uint_as_float(__float_as_uint(p0[r]) & sel_bit_mask(selw, r));
;     }
.LBB0_1816:
	v_cndmask_b32_e64 v197, v128, v184, s[2:3]
	v_mul_f32_e32 v172, 0xbe0293ee, v197
	v_fmamk_f32 v128, v96, 0x3e0293ee, v172
	v_fmamk_f32 v129, v97, 0x3e0293ee, v172
	v_fmamk_f32 v130, v98, 0x3e0293ee, v172
	v_fmamk_f32 v131, v99, 0x3e0293ee, v172
	v_fmamk_f32 v132, v100, 0x3e0293ee, v172
	v_fmamk_f32 v133, v101, 0x3e0293ee, v172
	v_fmamk_f32 v134, v102, 0x3e0293ee, v172
	v_fmamk_f32 v135, v103, 0x3e0293ee, v172
	v_fmamk_f32 v136, v104, 0x3e0293ee, v172
	v_fmamk_f32 v137, v105, 0x3e0293ee, v172
	v_fmamk_f32 v138, v106, 0x3e0293ee, v172
	v_fmamk_f32 v139, v107, 0x3e0293ee, v172
	v_fmamk_f32 v140, v108, 0x3e0293ee, v172
	v_fmamk_f32 v109, v109, 0x3e0293ee, v172
	v_fmamk_f32 v110, v110, 0x3e0293ee, v172
	v_fmamk_f32 v141, v111, 0x3e0293ee, v172
	v_fmamk_f32 v107, v80, 0x3e0293ee, v172
	v_fmamk_f32 v108, v81, 0x3e0293ee, v172
	v_fmamk_f32 v100, v82, 0x3e0293ee, v172
	v_fmamk_f32 v101, v83, 0x3e0293ee, v172
	v_fmamk_f32 v102, v84, 0x3e0293ee, v172
	v_fmamk_f32 v103, v85, 0x3e0293ee, v172
	v_fmamk_f32 v104, v86, 0x3e0293ee, v172
	v_fmamk_f32 v105, v87, 0x3e0293ee, v172
	v_fmamk_f32 v106, v88, 0x3e0293ee, v172
	v_fmamk_f32 v96, v89, 0x3e0293ee, v172
	v_fmamk_f32 v97, v90, 0x3e0293ee, v172
	v_fmamk_f32 v98, v91, 0x3e0293ee, v172
	v_fmamk_f32 v99, v92, 0x3e0293ee, v172
	v_exp_f32_e32 v80, v128
	v_exp_f32_e32 v81, v129
	v_exp_f32_e32 v82, v130
	v_exp_f32_e32 v83, v131
	v_exp_f32_e32 v84, v132
	v_exp_f32_e32 v85, v133
	v_exp_f32_e32 v86, v134
	v_exp_f32_e32 v87, v135
	v_exp_f32_e32 v88, v136
	v_exp_f32_e32 v89, v137
	v_exp_f32_e32 v90, v138
	v_exp_f32_e32 v91, v139
	v_exp_f32_e32 v92, v140
	v_exp_f32_e32 v128, v109
	v_exp_f32_e32 v111, v110
	v_exp_f32_e32 v129, v141
	v_fmamk_f32 v109, v93, 0x3e0293ee, v172
	v_fmamk_f32 v110, v94, 0x3e0293ee, v172
	v_fmac_f32_e32 v172, 0x3e0293ee, v95
	v_and_b32_e32 v81, v120, v81
	v_and_b32_e32 v80, v112, v80
	v_and_b32_e32 v83, v121, v83
	v_and_b32_e32 v82, v113, v82
	v_and_b32_e32 v85, v122, v85
	v_and_b32_e32 v84, v114, v84
	v_and_b32_e32 v87, v123, v87
	v_and_b32_e32 v86, v115, v86
	v_and_b32_e32 v89, v124, v89
	v_and_b32_e32 v88, v116, v88
	v_and_b32_e32 v91, v125, v91
	v_and_b32_e32 v90, v117, v90
	v_and_b32_e32 v93, v126, v128
	v_and_b32_e32 v92, v118, v92
	v_and_b32_e32 v95, v127, v129
	v_and_b32_e32 v94, v119, v111
	s_waitcnt lgkmcnt(0)
	s_barrier
; __device__ __forceinline__ unsigned sel_bit_mask(unsigned w, int b) { unsigned m; asm("v_bfe_i32 %0, %1, %2, 1" : "=v"(m) : "v"(w), "n"(b)); return m; }
; template <bool SEL>
; __device__ __forceinline__ void finishSM(f32x16& p0, f32x16& p1, float alpha, float& l_reg, bf16x8& pa0, bf16x8& pa1, bf16x8& pa2, bf16x8& pa3, unsigned selw) {
; #pragma unroll
;     for (int r = 0; r < 16; ++r) p1[r] = __builtin_amdgcn_exp2f(p1[r]);
;     if (SEL) {
; #pragma unroll
;         for (int r = 0; r < 16; ++r) p1[r] = __uint_as_float(__float_as_uint(p1[r]) & sel_bit_mask(selw, 16 + r));
;     }
;     float ps = 0;
; #pragma unroll
;     for (int r = 0; r < 16; ++r) ps += p0[r];
; #pragma unroll
;     for (int r = 0; r < 16; ++r) ps += p1[r];
;     { auto rr = __builtin_amdgcn_permlane32_swap(__float_as_uint(ps), __float_as_uint(ps), false, false);
;       ps = __uint_as_float(rr[0]) + __uint_as_float(rr[1]); }
;     l_reg = l_reg * alpha + ps;
;     ...
;     PK4(p0, 0, pa0); PK4(p0, 8, pa1); PK4(p1, 0, pa2); PK4(p1, 8, pa3);
;     ...
; }
; template <int KB, int QREG>
; __device__ __forceinline__ void qkt(f32x16& p0, f32x16& p1, const char* K_lds, int r32, int hi, const bf16x8* qr, const char* qlds) {
;     p0 = f32x16{}; p1 = f32x16{};
;     const char* kb[4];
; #pragma unroll
;     for (int dd = 0; dd < 4; ++dd) kb[dd] = K_lds + KB * SHM_K + KSWZ(r32, (dd * 16 + hi * 8) * 2);
; #pragma unroll
;     for (int d0 = 0; d0 < 8; ++d0) { const char* a = kb[d0 & 3] + (d0 >> 2) * 128;
;         bf16x8 b0 = *reinterpret_cast<const bf16x8*>(a);
;         bf16x8 b1 = *reinterpret_cast<const bf16x8*>(a + 32 * 256);
;         const bf16x8 qf = (d0 < QREG) ? qr[d0 < QREG ? d0 : 0] : *reinterpret_cast<const bf16x8*>(qlds + (d0 - QREG) * 1024);
;         p0 = __builtin_amdgcn_mfma_f32_32x32x16_bf16(b0, qf, p0, 0, 0, 0);
;         p1 = __builtin_amdgcn_mfma_f32_32x32x16_bf16(b1, qf, p1, 0, 0, 0); }
; }
	ds_read_b128 v[242:245], v208
	ds_read_b128 v[182:185], v208 offset:1024
	ds_read_b128 v[112:115], v213 offset:32768
	ds_read_b128 v[116:119], v213 offset:40960
	ds_read_b128 v[174:177], v212 offset:32768
	ds_read_b128 v[178:181], v212 offset:40960
	ds_read_b128 v[250:253], v211 offset:32768
	v_exp_f32_e32 v101, v101
	v_exp_f32_e32 v103, v103
	s_waitcnt lgkmcnt(4)
	v_mfma_f32_32x32x16_bf16 v[128:143], v[112:115], v[164:167], 0
	v_exp_f32_e32 v105, v105
	v_exp_f32_e32 v111, v96
	v_exp_f32_e32 v109, v109
	v_exp_f32_e32 v172, v172
	v_exp_f32_e32 v107, v107
	v_exp_f32_e32 v108, v108
	v_exp_f32_e32 v100, v100
	s_waitcnt lgkmcnt(3)
	v_mfma_f32_32x32x16_bf16 v[112:127], v[116:119], v[164:167], 0
	v_bfe_i32 v96, v217, 16, 1
	v_exp_f32_e32 v102, v102
	v_exp_f32_e32 v173, v97
	v_bfe_i32 v97, v217, 17, 1
	v_and_b32_e32 v96, v96, v107
	v_and_b32_e32 v97, v97, v108
	v_exp_f32_e32 v104, v104
	s_waitcnt lgkmcnt(2)
	v_mfma_f32_32x32x16_bf16 v[128:143], v[174:177], v[160:163], v[128:143]
	ds_read_b128 v[174:177], v211 offset:40960
	v_exp_f32_e32 v106, v106
	v_exp_f32_e32 v110, v110
	v_bfe_i32 v107, v217, 27, 1
	v_bfe_i32 v108, v217, 28, 1
	s_waitcnt lgkmcnt(2)
	v_mfma_f32_32x32x16_bf16 v[112:127], v[178:181], v[160:163], v[112:127]
	ds_read_b128 v[178:181], v210 offset:32768
	s_waitcnt lgkmcnt(2)
	v_mfma_f32_32x32x16_bf16 v[128:143], v[250:253], v[156:159], v[128:143]
	ds_read_b128 v[250:253], v210 offset:40960
	s_waitcnt lgkmcnt(2)
	v_mfma_f32_32x32x16_bf16 v[112:127], v[174:177], v[156:159], v[112:127]
	ds_read_b128 v[174:177], v213 offset:32896
	s_waitcnt lgkmcnt(2)
	v_mfma_f32_32x32x16_bf16 v[128:143], v[178:181], v[152:155], v[128:143]
	ds_read_b128 v[178:181], v213 offset:41088
	s_waitcnt lgkmcnt(2)
	v_mfma_f32_32x32x16_bf16 v[112:127], v[250:253], v[152:155], v[112:127]
	ds_read_b128 v[250:253], v212 offset:32896
	s_waitcnt lgkmcnt(2)
	v_mfma_f32_32x32x16_bf16 v[128:143], v[174:177], v[148:151], v[128:143]
	ds_read_b128 v[174:177], v212 offset:41088
	s_waitcnt lgkmcnt(2)
	v_mfma_f32_32x32x16_bf16 v[112:127], v[178:181], v[148:151], v[112:127]
	ds_read_b128 v[178:181], v211 offset:32896
	s_waitcnt lgkmcnt(2)
	v_mfma_f32_32x32x16_bf16 v[128:143], v[250:253], v[144:147], v[128:143]
	ds_read_b128 v[250:253], v211 offset:41088
	s_waitcnt lgkmcnt(2)
	v_mfma_f32_32x32x16_bf16 v[112:127], v[174:177], v[144:147], v[112:127]
	ds_read_b128 v[174:177], v210 offset:32896
	s_waitcnt lgkmcnt(2)
	v_mfma_f32_32x32x16_bf16 v[128:143], v[178:181], v[242:245], v[128:143]
	ds_read_b128 v[178:181], v210 offset:41088
	s_waitcnt lgkmcnt(2)
	v_mfma_f32_32x32x16_bf16 v[112:127], v[250:253], v[242:245], v[112:127]
	s_waitcnt lgkmcnt(1)
	v_mfma_f32_32x32x16_bf16 v[128:143], v[174:177], v[182:185], v[128:143]
	v_exp_f32_e32 v175, v99
	v_bfe_i32 v99, v217, 19, 1
	v_exp_f32_e32 v174, v98
	v_and_b32_e32 v99, v99, v101
	v_bfe_i32 v101, v217, 21, 1
	v_bfe_i32 v98, v217, 18, 1
	v_and_b32_e32 v107, v107, v174
	v_and_b32_e32 v101, v101, v103
	v_bfe_i32 v103, v217, 23, 1
	v_and_b32_e32 v98, v98, v100
	v_and_b32_e32 v103, v103, v105
	v_bfe_i32 v105, v217, 25, 1
	v_bfe_i32 v100, v217, 20, 1
	s_waitcnt lgkmcnt(0)
	v_mfma_f32_32x32x16_bf16 v[112:127], v[178:181], v[182:185], v[112:127]
	v_and_b32_e32 v105, v105, v111
	v_bfe_i32 v111, v217, 29, 1
	v_and_b32_e32 v100, v100, v102
	v_and_b32_e32 v109, v111, v109
	v_bfe_i32 v111, v217, 31, 1
	v_bfe_i32 v102, v217, 22, 1
	v_and_b32_e32 v108, v108, v175
	v_and_b32_e32 v111, v111, v172
	v_add_f32_e32 v172, 0, v80
	v_add_f32_e32 v172, v172, v81
	v_add_f32_e32 v172, v172, v82
	v_add_f32_e32 v172, v172, v83
	v_add_f32_e32 v172, v172, v84
	v_add_f32_e32 v172, v172, v85
	v_add_f32_e32 v172, v172, v86
	v_add_f32_e32 v172, v172, v87
	v_add_f32_e32 v172, v172, v88
	v_add_f32_e32 v172, v172, v89
	v_add_f32_e32 v172, v172, v90
	v_add_f32_e32 v172, v172, v91
	v_add_f32_e32 v172, v172, v92
	v_add_f32_e32 v172, v172, v93
	v_add_f32_e32 v172, v172, v94
	v_add_f32_e32 v172, v172, v95
	v_add_f32_e32 v172, v172, v96
	v_add_f32_e32 v172, v172, v97
	v_add_f32_e32 v172, v172, v98
	v_add_f32_e32 v172, v172, v99
	v_add_f32_e32 v172, v172, v100
	v_and_b32_e32 v102, v102, v104
	v_add_f32_e32 v172, v172, v101
	v_bfe_i32 v104, v217, 24, 1
	v_add_f32_e32 v172, v172, v102
	v_and_b32_e32 v104, v104, v106
	v_add_f32_e32 v172, v172, v103
	v_bfe_i32 v106, v217, 26, 1
	v_add_f32_e32 v172, v172, v104
	v_and_b32_e32 v106, v106, v173
	v_add_f32_e32 v172, v172, v105
	v_add_f32_e32 v172, v172, v106
	v_add_f32_e32 v172, v172, v107
	v_add_f32_e32 v172, v172, v108
	v_bfe_i32 v173, v217, 30, 1
	v_add_f32_e32 v172, v172, v109
	v_and_b32_e32 v110, v173, v110
	v_add_f32_e32 v172, v172, v110
	v_add_f32_e32 v220, v172, v111
	v_mov_b32_e32 v221, v220
	v_cvt_pk_bf16_f32 v172, v80, v81
	v_cvt_pk_bf16_f32 v173, v82, v83
	v_cvt_pk_bf16_f32 v174, v84, v85
	v_cvt_pk_bf16_f32 v175, v86, v87
	v_cvt_pk_bf16_f32 v176, v88, v89
	v_cvt_pk_bf16_f32 v177, v90, v91
	v_cvt_pk_bf16_f32 v178, v92, v93
	v_cvt_pk_bf16_f32 v179, v94, v95
	v_cvt_pk_bf16_f32 v180, v96, v97
	v_cvt_pk_bf16_f32 v181, v98, v99
	v_cvt_pk_bf16_f32 v182, v100, v101
	v_cvt_pk_bf16_f32 v183, v102, v103
	v_cvt_pk_bf16_f32 v184, v104, v105
	v_cvt_pk_bf16_f32 v185, v106, v107
	v_cvt_pk_bf16_f32 v186, v108, v109
	v_cvt_pk_bf16_f32 v187, v110, v111
	s_nop 1
	v_permlane32_swap_b32_e32 v220, v221
	v_permlane32_swap_b32_e32 v172, v174
	v_permlane32_swap_b32_e32 v173, v175
	v_permlane32_swap_b32_e32 v176, v178
	v_permlane32_swap_b32_e32 v177, v179
	v_permlane32_swap_b32_e32 v180, v182
	v_permlane32_swap_b32_e32 v181, v183
	v_permlane32_swap_b32_e32 v184, v186
	v_permlane32_swap_b32_e32 v185, v187
	v_mov_b32_e32 v195, v1
	v_lshl_add_u64 v[222:223], v[194:195], 2, s[44:45]
	global_load_dword v195, v[222:223], off
	s_add_i32 s2, s54, 1
	s_cmp_lt_i32 s2, s87
	s_cselect_b64 s[48:49], -1, 0
	s_cmp_ge_i32 s2, s87
	s_cbranch_scc1 .LBB0_1818
	v_add_u32_e32 v2, 64, v196
	v_add_u32_e32 v4, 0x60, v196
	v_ashrrev_i32_e32 v3, 31, v2
	v_ashrrev_i32_e32 v5, 31, v4
	v_lshlrev_b64 v[10:11], 10, v[2:3]
	v_lshlrev_b64 v[12:13], 10, v[4:5]
	v_lshl_add_u64 v[2:3], v[14:15], 0, v[10:11]
	v_lshl_add_u64 v[6:7], v[14:15], 0, v[12:13]
	v_lshl_add_u64 v[10:11], v[192:193], 0, v[10:11]
	v_lshl_add_u64 v[168:169], v[192:193], 0, v[12:13]
	global_load_dwordx4 v[2:5], v[2:3], off
	s_nop 0
	global_load_dwordx4 v[6:9], v[6:7], off
	s_nop 0
	global_load_dwordx4 v[10:13], v[10:11], off
	s_nop 0
	global_load_dwordx4 v[168:171], v[168:169], off
